# phase M: the 8 gate-vector loads of a row issued together (were 4 dependent 2-load round trips)
# speedup vs baseline: 1.0028x; 1.0013x over previous
; #define M_UNPACK(dst, v) do { dst[0] = bflo(v.x); dst[1] = bfhi(v.x); dst[2] = bflo(v.y); dst[3] = bfhi(v.y); dst[4] = bflo(v.z); dst[5] = bfhi(v.z); dst[6] = bflo(v.w); dst[7] = bfhi(v.w); } while (0)
; __device__ __forceinline__ void ph_combine(const Params& p, int l) {
;     ...
;         for (int j = 0; j < 4; ++j) { M_UNPACK(x[j], xv[j]);
; #pragma unroll
;             for (int i = 0; i < 8; ++i) s[j][i] = 0.f; }
;         unsigned msk = (unsigned)__ballot(myinv >= 0);
;         while (msk) {
;             const int e0 = __builtin_ctz(msk); msk &= msk - 1; const bool two = msk != 0u; const int e1 = two ? __builtin_ctz(msk) : e0; if (two) msk &= msk - 1;
;             const int r0 = __shfl(myinv, e0), r1 = __shfl(myinv, e1);
;             const bf16_t* y0 = YS + ((size_t)e0 * EROWS + r0) * DM + lane * 8; const bf16_t* y1 = YS + ((size_t)e1 * EROWS + r1) * DM + lane * 8;
;             u32x4 v0[4], v1[4];
; #pragma unroll
;             for (int j = 0; j < 4; ++j) { v0[j] = *(const u32x4*)(y0 + j * 512); v1[j] = *(const u32x4*)(y1 + j * 512); }
;             const float f1 = two ? 1.0f : 0.0f;
; #pragma unroll
;             for (int j = 0; j < 4; ++j) { float a[8], b[8]; M_UNPACK(a, v0[j]); M_UNPACK(b, v1[j]);
; #pragma unroll
;                 for (int i = 0; i < 8; ++i) s[j][i] += a[i] + f1 * b[i]; }
;         }
;         const float* gate = mod + (size_t)(l * 5 + rr) * 12288 + 5 * DM + lane * 8;
;         float ss = 0.f;
; #pragma unroll
;         for (int j = 0; j < 4; ++j) { const f32x4 g0 = *(const f32x4*)(gate + j * 512), g1 = *(const f32x4*)(gate + j * 512 + 4);
; #pragma unroll
;             for (int i = 0; i < 8; ++i) { x[j][i] += (i < 4 ? g0[i] : g1[i - 4]) * s[j][i]; ss += x[j][i] * x[j][i]; } }
;         ss = wave_sum(ss); const float rinv = rsqrtf(ss * (1.0f / DM) + EPS);
.LBB0_2689:
	v_lshlrev_b32_e32 v118, 16, v30
	v_and_b32_e32 v119, 0xffff0000, v30
	v_lshl_add_u32 v30, s25, 3, v124
	v_lshlrev_b32_e32 v116, 16, v32
	v_and_b32_e32 v117, 0xffff0000, v32
	v_lshlrev_b32_e32 v114, 16, v33
	v_and_b32_e32 v115, 0xffff0000, v33
	v_lshlrev_b32_e32 v32, 16, v20
	v_and_b32_e32 v33, 0xffff0000, v20
	v_min_i32_e32 v20, 0x2000, v30
	v_ashrrev_i32_e32 v120, 11, v20
	v_add_u32_e32 v20, s13, v120
	v_lshlrev_b32_e32 v98, 16, v18
	v_and_b32_e32 v99, 0xffff0000, v18
	v_lshlrev_b32_e32 v96, 16, v19
	v_and_b32_e32 v97, 0xffff0000, v19
	v_lshlrev_b32_e32 v18, 16, v21
	v_and_b32_e32 v19, 0xffff0000, v21
	v_mul_hi_i32_i24_e32 v21, 0xc000, v20
	v_mul_i32_i24_e32 v20, 0xc000, v20
	v_lshl_add_u64 v[20:21], s[2:3], 0, v[20:21]
	v_lshl_add_u64 v[122:123], v[20:21], 0, v[206:207]
	s_mov_b64 s[0:1], 0xa000
	v_lshl_add_u64 v[138:139], v[122:123], 0, s[0:1]
	s_mov_b32 s0, 0xb000
	v_add_co_u32_e32 v140, vcc, s0, v122
	v_lshlrev_b32_e32 v94, 16, v22
	s_nop 0
	v_addc_co_u32_e32 v141, vcc, 0, v123, vcc
	v_and_b32_e32 v95, 0xffff0000, v22
	v_lshlrev_b32_e32 v92, 16, v23
	v_and_b32_e32 v93, 0xffff0000, v23
	global_load_dwordx4 v[148:151], v[140:141], off offset:-4096
	global_load_dwordx4 v[152:155], v[138:139], off offset:16
	global_load_dwordx4 v[156:159], v[138:139], off offset:2064
	global_load_dwordx4 v[160:163], v[138:139], off offset:2048
	global_load_dwordx4 v[164:167], v[140:141], off
	global_load_dwordx4 v[168:171], v[140:141], off offset:16
	global_load_dwordx4 v[172:175], v[140:141], off offset:2048
	global_load_dwordx4 v[176:179], v[140:141], off offset:2064
	v_lshlrev_b32_e32 v108, 16, v31
	v_and_b32_e32 v109, 0xffff0000, v31
	v_lshlrev_b32_e32 v112, 16, v26
	v_and_b32_e32 v113, 0xffff0000, v26
	v_lshlrev_b32_e32 v110, 16, v27
	v_and_b32_e32 v111, 0xffff0000, v27
	v_lshlrev_b32_e32 v106, 16, v28
	v_and_b32_e32 v107, 0xffff0000, v28
	v_lshlrev_b32_e32 v104, 16, v29
	v_and_b32_e32 v105, 0xffff0000, v29
	v_lshlrev_b32_e32 v102, 16, v24
	v_and_b32_e32 v103, 0xffff0000, v24
	v_lshlrev_b32_e32 v100, 16, v25
	v_and_b32_e32 v101, 0xffff0000, v25
	s_mov_b64 s[0:1], 0xb000
	v_readlane_b32 s14, v255, 57
	v_readlane_b32 s15, v255, 58
	v_ashrrev_i32_e32 v31, 31, v30
	s_waitcnt vmcnt(7)
	v_pk_fma_f32 v[28:29], v[90:91], v[148:149], v[118:119]
	v_pk_fma_f32 v[26:27], v[88:89], v[150:151], v[108:109]
	s_waitcnt vmcnt(6)
	v_pk_fma_f32 v[24:25], v[60:61], v[152:153], v[116:117]
	v_pk_fma_f32 v[22:23], v[58:59], v[154:155], v[114:115]
	v_pk_mul_f32 v[20:21], v[28:29], v[28:29]
	v_pk_mul_f32 v[108:109], v[26:27], v[26:27]
	v_add_f32_e32 v20, v20, v21
	v_add_f32_e32 v20, v108, v20
	v_pk_mul_f32 v[60:61], v[24:25], v[24:25]
	v_add_f32_e32 v20, v109, v20
	v_add_f32_e32 v20, v60, v20
	v_pk_mul_f32 v[58:59], v[22:23], v[22:23]
	v_add_f32_e32 v20, v61, v20
	v_add_f32_e32 v20, v58, v20
	v_add_f32_e32 v20, v59, v20
	s_waitcnt vmcnt(5)
	v_pk_fma_f32 v[106:107], v[52:53], v[156:157], v[106:107]
	s_waitcnt vmcnt(4)
	v_pk_fma_f32 v[112:113], v[56:57], v[160:161], v[112:113]
	v_lshl_add_u64 v[114:115], v[122:123], 0, s[0:1]
	v_pk_fma_f32 v[110:111], v[54:55], v[162:163], v[110:111]
	v_pk_fma_f32 v[104:105], v[50:51], v[158:159], v[104:105]
	s_nop 0
	s_mov_b64 s[0:1], 0xb800
	v_pk_mul_f32 v[56:57], v[112:113], v[112:113]
	v_pk_mul_f32 v[54:55], v[110:111], v[110:111]
	v_add_f32_e32 v20, v56, v20
	v_add_f32_e32 v20, v57, v20
	v_add_f32_e32 v20, v54, v20
	v_pk_mul_f32 v[52:53], v[106:107], v[106:107]
	v_add_f32_e32 v20, v55, v20
	v_add_f32_e32 v20, v52, v20
	v_pk_mul_f32 v[50:51], v[104:105], v[104:105]
	v_add_f32_e32 v20, v53, v20
	v_add_f32_e32 v20, v50, v20
	v_add_f32_e32 v20, v51, v20
	s_waitcnt vmcnt(3)
	v_pk_fma_f32 v[92:93], v[46:47], v[166:167], v[92:93]
	s_waitcnt vmcnt(2)
	v_pk_fma_f32 v[90:91], v[44:45], v[168:169], v[102:103]
	v_lshl_add_u64 v[114:115], v[122:123], 0, s[0:1]
	v_pk_fma_f32 v[94:95], v[48:49], v[164:165], v[94:95]
	v_pk_fma_f32 v[88:89], v[42:43], v[170:171], v[100:101]
	s_nop 0
	v_pk_mul_f32 v[48:49], v[94:95], v[94:95]
	v_pk_mul_f32 v[46:47], v[92:93], v[92:93]
	v_add_f32_e32 v20, v48, v20
	v_add_f32_e32 v20, v49, v20
	v_add_f32_e32 v20, v46, v20
	v_pk_mul_f32 v[44:45], v[90:91], v[90:91]
	v_add_f32_e32 v20, v47, v20
	v_add_f32_e32 v20, v44, v20
	v_pk_mul_f32 v[42:43], v[88:89], v[88:89]
	v_add_f32_e32 v20, v45, v20
	v_add_f32_e32 v20, v42, v20
	v_add_f32_e32 v20, v43, v20
	s_mov_b32 s0, 0x800000
	s_waitcnt vmcnt(1)
	v_pk_fma_f32 v[98:99], v[40:41], v[172:173], v[98:99]
	s_nop 0
	v_pk_mul_f32 v[40:41], v[98:99], v[98:99]
	v_pk_fma_f32 v[96:97], v[38:39], v[174:175], v[96:97]
	v_add_f32_e32 v20, v40, v20
	v_pk_mul_f32 v[38:39], v[96:97], v[96:97]
	v_add_f32_e32 v20, v41, v20
	s_waitcnt vmcnt(0)
	v_pk_fma_f32 v[102:103], v[36:37], v[176:177], v[32:33]
	v_add_f32_e32 v20, v38, v20
	v_pk_mul_f32 v[32:33], v[102:103], v[102:103]
	v_add_f32_e32 v20, v39, v20
	v_pk_fma_f32 v[100:101], v[34:35], v[178:179], v[18:19]
	v_add_f32_e32 v20, v32, v20
	v_pk_mul_f32 v[18:19], v[100:101], v[100:101]
	v_add_f32_e32 v20, v33, v20
	v_add_f32_e32 v18, v18, v20
	v_add_f32_e32 v18, v19, v18
	v_mov_b32_e32 v19, v18
	s_nop 1
	v_permlane32_swap_b32_e32 v19, v18
	s_waitcnt lgkmcnt(0)
	v_add_f32_e32 v18, v18, v19
	v_mov_b32_e32 v19, v18
	s_nop 1
	v_permlane16_swap_b32_e32 v19, v18
	s_waitcnt lgkmcnt(0)
	v_add_f32_e32 v18, v18, v19
	s_nop 1
	v_mov_b32_dpp v19, v18 row_ror:8 row_mask:0xf bank_mask:0xf
	s_waitcnt lgkmcnt(0)
	v_add_f32_e32 v18, v18, v19
	s_nop 1
	v_mov_b32_dpp v19, v18 row_shl:4 row_mask:0xf bank_mask:0x5
	v_mov_b32_dpp v19, v18 row_shr:4 row_mask:0xf bank_mask:0xa
	s_waitcnt lgkmcnt(0)
	v_add_f32_e32 v18, v18, v19
	s_nop 1
	v_mov_b32_dpp v19, v18 quad_perm:[2,3,0,1] row_mask:0xf bank_mask:0xf
	s_waitcnt lgkmcnt(0)
	v_add_f32_e32 v18, v18, v19
	s_nop 1
	v_mov_b32_dpp v19, v18 quad_perm:[1,0,3,2] row_mask:0xf bank_mask:0xf
	s_waitcnt lgkmcnt(0)
	v_add_f32_e32 v18, v18, v19
	v_fmamk_f32 v18, v18, 0x3a000000, v246
	v_cmp_gt_f32_e32 vcc, s0, v18
	v_mul_f32_e32 v19, 0x4b800000, v18
	s_mov_b64 s[0:1], -1
	v_cndmask_b32_e32 v18, v18, v19, vcc
	v_rsq_f32_e32 v18, v18
	s_nop 0
	v_mul_f32_e32 v19, 0x45800000, v18
	v_cndmask_b32_e32 v108, v18, v19, vcc
	s_and_b64 vcc, exec, s[14:15]
	s_cbranch_vccz .LBB0_2691
; __device__ __forceinline__ void ph_combine(const Params& p, int l) {
;     ...
;             float* orow = p.out + (size_t)row * DM + lane * 8; const float* g = p.in[I_FNG] + lane * 8;
;             f32x4 gq[8];
; #pragma unroll
;             for (int j = 0; j < 4; ++j) { gq[2 * j] = *(const f32x4*)(g + j * 512); gq[2 * j + 1] = *(const f32x4*)(g + j * 512 + 4); }
; #pragma unroll
;             for (int j = 0; j < 4; ++j) { const f32x4 ga = gq[2 * j], gb = gq[2 * j + 1];
;                 *(f32x4*)(orow + j * 512) = (f32x4){x[j][0] * rinv * ga[0], x[j][1] * rinv * ga[1], x[j][2] * rinv * ga[2], x[j][3] * rinv * ga[3]};
;                 *(f32x4*)(orow + j * 512 + 4) = (f32x4){x[j][4] * rinv * gb[0], x[j][5] * rinv * gb[1], x[j][6] * rinv * gb[2], x[j][7] * rinv * gb[3]}; }
	global_load_dwordx4 v[32:35], v[76:77], off offset:16
	global_load_dwordx4 v[36:39], v[76:77], off
	global_load_dwordx4 v[40:43], v[76:77], off offset:2064
	global_load_dwordx4 v[44:47], v[76:77], off offset:2048
	global_load_dwordx4 v[48:51], v[78:79], off offset:16
	global_load_dwordx4 v[52:55], v[78:79], off
	global_load_dwordx4 v[18:21], v[80:81], off offset:16
	global_load_dwordx4 v[56:59], v[80:81], off
	v_lshlrev_b64 v[60:61], 13, v[30:31]
	v_pk_mul_f32 v[114:115], v[28:29], v[108:109] op_sel_hi:[1,0]
	v_pk_mul_f32 v[116:117], v[26:27], v[108:109] op_sel_hi:[1,0]
	v_lshl_add_u64 v[60:61], v[74:75], 0, v[60:61]
	s_movk_i32 s0, 0x1000
	s_waitcnt vmcnt(6)
	v_pk_mul_f32 v[38:39], v[116:117], v[38:39]
	v_pk_mul_f32 v[36:37], v[114:115], v[36:37]
	global_store_dwordx4 v[60:61], v[36:39], off
	s_nop 1
	v_pk_mul_f32 v[36:37], v[24:25], v[108:109] op_sel_hi:[1,0]
	v_pk_mul_f32 v[38:39], v[22:23], v[108:109] op_sel_hi:[1,0]
	v_pk_mul_f32 v[32:33], v[36:37], v[32:33]
	v_pk_mul_f32 v[34:35], v[38:39], v[34:35]
	global_store_dwordx4 v[60:61], v[32:35], off offset:16
	v_add_co_u32_e32 v36, vcc, s0, v60
	s_nop 0
	v_pk_mul_f32 v[32:33], v[112:113], v[108:109] op_sel_hi:[1,0]
	v_pk_mul_f32 v[34:35], v[110:111], v[108:109] op_sel_hi:[1,0]
	s_waitcnt vmcnt(6)
	v_pk_mul_f32 v[32:33], v[32:33], v[44:45]
	v_pk_mul_f32 v[34:35], v[34:35], v[46:47]
	global_store_dwordx4 v[60:61], v[32:35], off offset:2048
	v_addc_co_u32_e32 v37, vcc, 0, v61, vcc
	s_nop 0
	v_pk_mul_f32 v[32:33], v[106:107], v[108:109] op_sel_hi:[1,0]
	v_pk_mul_f32 v[34:35], v[104:105], v[108:109] op_sel_hi:[1,0]
	v_pk_mul_f32 v[32:33], v[32:33], v[40:41]
	v_pk_mul_f32 v[34:35], v[34:35], v[42:43]
	global_store_dwordx4 v[60:61], v[32:35], off offset:2064
	s_mov_b64 s[0:1], 0
	s_nop 0
	v_pk_mul_f32 v[32:33], v[94:95], v[108:109] op_sel_hi:[1,0]
	v_pk_mul_f32 v[34:35], v[92:93], v[108:109] op_sel_hi:[1,0]
	s_waitcnt vmcnt(6)
	v_pk_mul_f32 v[32:33], v[32:33], v[52:53]
	v_pk_mul_f32 v[34:35], v[34:35], v[54:55]
	global_store_dwordx4 v[36:37], v[32:35], off
	s_nop 1
	v_pk_mul_f32 v[32:33], v[90:91], v[108:109] op_sel_hi:[1,0]
	v_pk_mul_f32 v[34:35], v[88:89], v[108:109] op_sel_hi:[1,0]
	v_pk_mul_f32 v[32:33], v[32:33], v[48:49]
	v_pk_mul_f32 v[34:35], v[34:35], v[50:51]
	global_store_dwordx4 v[36:37], v[32:35], off offset:16
	s_nop 1
	v_pk_mul_f32 v[32:33], v[98:99], v[108:109] op_sel_hi:[1,0]
	v_pk_mul_f32 v[34:35], v[96:97], v[108:109] op_sel_hi:[1,0]
	s_waitcnt vmcnt(6)
	v_pk_mul_f32 v[32:33], v[32:33], v[56:57]
	v_pk_mul_f32 v[34:35], v[34:35], v[58:59]
	global_store_dwordx4 v[36:37], v[32:35], off offset:2048
	s_nop 1
	v_pk_mul_f32 v[32:33], v[102:103], v[108:109] op_sel_hi:[1,0]
	v_pk_mul_f32 v[34:35], v[100:101], v[108:109] op_sel_hi:[1,0]
	v_pk_mul_f32 v[18:19], v[32:33], v[18:19]
	v_pk_mul_f32 v[20:21], v[34:35], v[20:21]
	global_store_dwordx4 v[36:37], v[18:21], off offset:2064
